# baseline (speedup 1.0000x reference)
_Z9gemm_gldsILi128ELi128ELi4ELi2ELi3ELi8ELi4ELi1ELi4096ELi1024ELi1024EEvPKDF16_S1_PfPKfS4_PKiPDF16_S7_S7_:
	s_load_dwordx4 s[4:7], s[0:1], 0x0
	s_load_dwordx2 s[8:9], s[0:1], 0x10
	s_ashr_i32 s0, s2, 3
	s_lshr_b32 s3, s0, 29
	s_add_i32 s3, s0, s3
	s_lshl_b32 s1, s2, 2
	s_lshr_b32 s10, s3, 3
	s_and_b32 s3, s3, 0x1fffff8
	s_and_b32 s2, s1, 24
	s_sub_i32 s0, s0, s3
	s_add_i32 s2, s2, s0
	s_and_b32 s0, s1, 4
	s_add_i32 s0, s0, s10
	s_lshl_b32 s2, s2, 7
	s_lshl_b32 s0, s0, 7
	v_lshlrev_b32_e32 v66, 4, v0
	v_and_b32_e32 v1, 32, v0
	s_ashr_i32 s3, s2, 31
	s_ashr_i32 s1, s0, 31
	v_lshrrev_b32_e32 v2, 3, v0
	v_bfe_u32 v30, v0, 2, 4
	v_bitop3_b32 v1, v66, v1, 48 bitop3:0x6c
	s_lshl_b64 s[10:11], s[2:3], 11
	s_lshl_b64 s[12:13], s[0:1], 11
	v_and_or_b32 v2, v2, 48, v30
	v_and_or_b32 v31, v0, 64, v1
	s_waitcnt lgkmcnt(0)
	s_add_u32 s4, s4, s10
	s_addc_u32 s5, s5, s11
	v_lshrrev_b32_e32 v2, 3, v0
	v_and_b32_e32 v31, 7, v2
	v_and_b32_e32 v30, 7, v0
	v_xor_b32_e32 v31, v30, v31
	v_lshlrev_b32_e32 v31, 4, v31
	v_lshl_or_b32 v2, v2, 11, v31
	v_mov_b32_e32 v94, v2
	v_mov_b32_e32 v3, 0
	v_readfirstlane_b32 s3, v66
	v_or_b32_e32 v1, 0x2000, v66
	s_add_u32 s6, s6, s12
	v_lshl_add_u64 v[4:5], s[4:5], 0, v[2:3]
	s_mov_b32 m0, s3
	s_mov_b64 s[10:11], 0x20000
	v_readfirstlane_b32 s3, v1
	v_or_b32_e32 v1, 0x4000, v66
	s_addc_u32 s7, s7, s13
	global_load_lds_dwordx4 v2, s[4:5]
	v_lshl_add_u64 v[8:9], v[4:5], 0, s[10:11]
	s_mov_b32 m0, s3
	v_readfirstlane_b32 s3, v1
	v_or_b32_e32 v1, 0x6000, v66
	v_lshl_add_u64 v[6:7], s[6:7], 0, v[2:3]
	global_load_lds_dwordx4 v[8:9], off
	s_mov_b32 m0, s3
	v_readfirstlane_b32 s3, v1
	v_or_b32_e32 v1, 0x8000, v66
	global_load_lds_dwordx4 v2, s[6:7]
	v_lshl_add_u64 v[8:9], v[6:7], 0, s[10:11]
	s_mov_b32 m0, s3
	s_mov_b64 s[10:11], 0x80
	v_readfirstlane_b32 s3, v1
	v_or_b32_e32 v1, 0xa000, v66
	global_load_lds_dwordx4 v[8:9], off
	v_lshl_add_u64 v[8:9], v[4:5], 0, s[10:11]
	s_mov_b32 m0, s3
	s_mov_b64 s[12:13], 0x20080
	v_readfirstlane_b32 s3, v1
	v_or_b32_e32 v1, 0xc000, v66
	global_load_lds_dwordx4 v[8:9], off
	v_lshl_add_u64 v[8:9], v[4:5], 0, s[12:13]
	s_mov_b32 m0, s3
	v_readfirstlane_b32 s3, v1
	v_or_b32_e32 v1, 0xe000, v66
	global_load_lds_dwordx4 v[8:9], off
	v_lshl_add_u64 v[8:9], v[6:7], 0, s[10:11]
	s_mov_b32 m0, s3
	v_readfirstlane_b32 s3, v1
	v_or_b32_e32 v1, 0x10000, v66
	global_load_lds_dwordx4 v[8:9], off
	v_lshl_add_u64 v[8:9], v[6:7], 0, s[12:13]
	s_mov_b32 m0, s3
	s_mov_b64 s[10:11], 0x100
	v_readfirstlane_b32 s3, v1
	v_or_b32_e32 v1, 0x12000, v66
	global_load_lds_dwordx4 v[8:9], off
	v_lshl_add_u64 v[8:9], v[4:5], 0, s[10:11]
	s_mov_b32 m0, s3
	s_mov_b64 s[12:13], 0x20100
	v_readfirstlane_b32 s3, v1
	v_or_b32_e32 v1, 0x14000, v66
	global_load_lds_dwordx4 v[8:9], off
	v_lshl_add_u64 v[4:5], v[4:5], 0, s[12:13]
	s_mov_b32 m0, s3
	v_readfirstlane_b32 s3, v1
	v_or_b32_e32 v1, 0x16000, v66
	global_load_lds_dwordx4 v[4:5], off
	v_lshl_add_u64 v[4:5], v[6:7], 0, s[10:11]
	s_mov_b32 m0, s3
	v_readfirstlane_b32 s3, v1
	global_load_lds_dwordx4 v[4:5], off
	v_lshl_add_u64 v[4:5], v[6:7], 0, s[12:13]
	s_mov_b32 m0, s3
	v_lshrrev_b32_e32 v63, 7, v0
	global_load_lds_dwordx4 v[4:5], off
	v_and_b32_e32 v2, 48, v0
	v_lshlrev_b32_e32 v4, 6, v0
	s_movk_i32 s3, 0x3c0
	v_lshlrev_b32_e32 v5, 2, v0
	v_bfe_u32 v62, v0, 6, 1
	v_and_or_b32 v2, v4, s3, v2
	v_lshlrev_b32_e32 v4, 12, v63
	v_and_b32_e32 v5, 32, v5
	v_and_b32_e32 v2, 15, v0
	v_bfe_u32 v5, v0, 4, 2
	v_and_b32_e32 v92, 7, v2
	v_xor_b32_e32 v5, v5, v92
	v_lshlrev_b32_e32 v5, 4, v5
	v_lshl_or_b32 v2, v2, 7, v5
	v_mov_b32_e32 v5, 0
	v_bitop3_b32 v65, v4, v2, v5 bitop3:0xf6
	v_lshlrev_b32_e32 v4, 13, v62
	v_lshrrev_b32_e32 v1, 2, v0
	v_bitop3_b32 v64, v4, v2, v5 bitop3:0xf6
	v_xor_b32_e32 v92, 64, v65
	v_xor_b32_e32 v93, 64, v64
	v_mov_b32_e32 v32, v3
	v_mov_b32_e32 v33, v3
	v_mov_b32_e32 v34, v3
	v_mov_b32_e32 v35, v3
	v_mov_b32_e32 v36, v3
	v_mov_b32_e32 v37, v3
	v_mov_b32_e32 v38, v3
	v_mov_b32_e32 v39, v3
	v_mov_b32_e32 v40, v3
	v_mov_b32_e32 v41, v3
	v_mov_b32_e32 v42, v3
	v_mov_b32_e32 v43, v3
	v_mov_b32_e32 v44, v3
	v_mov_b32_e32 v45, v3
	v_mov_b32_e32 v46, v3
	v_mov_b32_e32 v47, v3
	v_mov_b32_e32 v48, v3
	v_mov_b32_e32 v49, v3
	v_mov_b32_e32 v50, v3
	v_mov_b32_e32 v51, v3
	v_mov_b32_e32 v52, v3
	v_mov_b32_e32 v53, v3
	v_mov_b32_e32 v54, v3
	v_mov_b32_e32 v55, v3
	v_mov_b32_e32 v56, v3
	v_mov_b32_e32 v57, v3
	s_waitcnt vmcnt(8) lgkmcnt(0)
	s_barrier
	ds_read_b128 v[10:13], v65
	ds_read_b128 v[6:9], v65 offset:2048
	ds_read_b128 v[22:25], v64 offset:16384
	ds_read_b128 v[18:21], v64 offset:18432
	ds_read_b128 v[26:29], v64 offset:20480
	ds_read_b128 v[14:17], v64 offset:22528
	v_mov_b32_e32 v2, v94
	v_lshl_add_u64 v[58:59], s[6:7], 0, v[2:3]
	v_lshl_add_u64 v[60:61], s[4:5], 0, v[2:3]
	s_mov_b32 s3, 0
	s_mov_b64 s[4:5], 0
	s_mov_b64 s[6:7], 0x180
	s_mov_b64 s[10:11], 0x20180
	v_mov_b32_e32 v2, v3
	v_mov_b32_e32 v4, v3
	v_mov_b32_e32 v5, v3
	v_mov_b32_e32 v30, v3
	v_mov_b32_e32 v31, v3
.LBB3_1:
	s_lshl_b32 s12, s3, 15
	v_or_b32_e32 v67, s12, v92
	s_waitcnt lgkmcnt(0)
	v_mfma_f32_16x16x32_f16 v[54:57], v[22:25], v[10:13], v[54:57]
	ds_read_b128 v[68:71], v67
	ds_read_b128 v[72:75], v67 offset:2048
	v_or_b32_e32 v67, s12, v93
	v_mfma_f32_16x16x32_f16 v[50:53], v[18:21], v[10:13], v[50:53]
	ds_read_b128 v[76:79], v67 offset:16384
	ds_read_b128 v[80:83], v67 offset:18432
	s_add_i32 s3, s3, 1
	v_mfma_f32_16x16x32_f16 v[46:49], v[26:29], v[10:13], v[46:49]
	ds_read_b128 v[84:87], v67 offset:20480
	ds_read_b128 v[88:91], v67 offset:22528
	v_mfma_f32_16x16x32_f16 v[42:45], v[14:17], v[10:13], v[42:45]
	v_mfma_f32_16x16x32_f16 v[38:41], v[22:25], v[6:9], v[38:41]
	v_mfma_f32_16x16x32_f16 v[34:37], v[18:21], v[6:9], v[34:37]
	v_mfma_f32_16x16x32_f16 v[30:33], v[26:29], v[6:9], v[30:33]
	v_mfma_f32_16x16x32_f16 v[2:5], v[14:17], v[6:9], v[2:5]
	v_or_b32_e32 v10, s12, v66
	v_lshl_add_u64 v[6:7], v[60:61], 0, s[4:5]
	v_readfirstlane_b32 s12, v10
	v_lshl_add_u64 v[8:9], v[6:7], 0, s[6:7]
	s_mov_b32 m0, s12
	s_waitcnt vmcnt(4) lgkmcnt(0)
	s_barrier
	global_load_lds_dwordx4 v[8:9], off
	v_or_b32_e32 v8, 0x2000, v10
	v_lshl_add_u64 v[6:7], v[6:7], 0, s[10:11]
	v_readfirstlane_b32 s12, v8
	s_mov_b32 m0, s12
	v_or_b32_e32 v11, 0x4000, v10
	global_load_lds_dwordx4 v[6:7], off
	v_lshl_add_u64 v[6:7], v[58:59], 0, s[4:5]
	v_readfirstlane_b32 s12, v11
	v_lshl_add_u64 v[8:9], v[6:7], 0, s[6:7]
	s_mov_b32 m0, s12
	v_lshl_add_u64 v[6:7], v[6:7], 0, s[10:11]
	global_load_lds_dwordx4 v[8:9], off
	v_or_b32_e32 v8, 0x6000, v10
	s_cmp_lg_u32 s3, 3
	v_readfirstlane_b32 s12, v8
	s_mov_b32 m0, s12
	s_cselect_b32 s3, s3, 0
	global_load_lds_dwordx4 v[6:7], off
	s_lshl_b32 s12, s3, 15
	v_or_b32_e32 v6, s12, v65
	v_or_b32_e32 v14, s12, v64
	s_waitcnt lgkmcnt(0)
	v_mfma_f32_16x16x32_f16 v[54:57], v[76:79], v[68:71], v[54:57]
	ds_read_b128 v[10:13], v6
	ds_read_b128 v[6:9], v6 offset:2048
	v_mfma_f32_16x16x32_f16 v[50:53], v[80:83], v[68:71], v[50:53]
	ds_read_b128 v[22:25], v14 offset:16384
	ds_read_b128 v[18:21], v14 offset:18432
	v_mfma_f32_16x16x32_f16 v[46:49], v[84:87], v[68:71], v[46:49]
	ds_read_b128 v[26:29], v14 offset:20480
	ds_read_b128 v[14:17], v14 offset:22528
	v_mfma_f32_16x16x32_f16 v[42:45], v[88:91], v[68:71], v[42:45]
	v_mfma_f32_16x16x32_f16 v[38:41], v[76:79], v[72:75], v[38:41]
	v_mfma_f32_16x16x32_f16 v[34:37], v[80:83], v[72:75], v[34:37]
	v_mfma_f32_16x16x32_f16 v[30:33], v[84:87], v[72:75], v[30:33]
	v_mfma_f32_16x16x32_f16 v[2:5], v[88:91], v[72:75], v[2:5]
	s_add_u32 s4, s4, 0x80
	s_addc_u32 s5, s5, 0
	s_cmpk_eq_i32 s4, 0x680
	s_cbranch_scc0 .LBB3_1
	s_waitcnt lgkmcnt(0)
	v_mfma_f32_16x16x32_f16 v[54:57], v[22:25], v[10:13], v[54:57]
	ds_read_b128 v[58:61], v92 offset:32768
	ds_read_b128 v[66:69], v92 offset:34816
	v_mfma_f32_16x16x32_f16 v[50:53], v[18:21], v[10:13], v[50:53]
	ds_read_b128 v[70:73], v93 offset:49152
	ds_read_b128 v[74:77], v93 offset:51200
	v_mfma_f32_16x16x32_f16 v[46:49], v[26:29], v[10:13], v[46:49]
	ds_read_b128 v[78:81], v93 offset:53248
	ds_read_b128 v[82:85], v93 offset:55296
	v_mfma_f32_16x16x32_f16 v[10:13], v[14:17], v[10:13], v[42:45]
	v_mfma_f32_16x16x32_f16 v[22:25], v[22:25], v[6:9], v[38:41]
	v_mfma_f32_16x16x32_f16 v[18:21], v[18:21], v[6:9], v[34:37]
	v_mfma_f32_16x16x32_f16 v[26:29], v[26:29], v[6:9], v[30:33]
	v_mfma_f32_16x16x32_f16 v[2:5], v[14:17], v[6:9], v[2:5]
	v_or_b32_e32 v14, 0x10000, v65
	s_nop 0
	v_add_u32_e32 v30, 0x10800, v65
	s_waitcnt vmcnt(4) lgkmcnt(0)
	s_barrier
	s_waitcnt lgkmcnt(0)
	v_mfma_f32_16x16x32_f16 v[6:9], v[70:73], v[58:61], v[54:57]
	ds_read_b128 v[14:17], v14
	ds_read_b128 v[30:33], v30
	v_or_b32_e32 v38, 0x14000, v64
	v_mfma_f32_16x16x32_f16 v[34:37], v[74:77], v[58:61], v[50:53]
	v_add_u32_e32 v42, 0x14800, v64
	v_add_u32_e32 v54, 0x15800, v64
	ds_read_b128 v[38:41], v38
	v_add_u32_e32 v50, 0x15000, v64
	ds_read_b128 v[42:45], v42
	v_mfma_f32_16x16x32_f16 v[46:49], v[78:81], v[58:61], v[46:49]
	ds_read_b128 v[50:53], v50
	ds_read_b128 v[54:57], v54
	v_mfma_f32_16x16x32_f16 v[10:13], v[82:85], v[58:61], v[10:13]
	v_mfma_f32_16x16x32_f16 v[22:25], v[70:73], v[66:69], v[22:25]
	v_mfma_f32_16x16x32_f16 v[18:21], v[74:77], v[66:69], v[18:21]
	v_mfma_f32_16x16x32_f16 v[26:29], v[78:81], v[66:69], v[26:29]
	v_mfma_f32_16x16x32_f16 v[2:5], v[82:85], v[66:69], v[2:5]
	v_add_u32_e32 v58, 0x10000, v92
	v_add_u32_e32 v66, 0x10800, v92
	v_add_u32_e32 v70, 0x14000, v93
	v_add_u32_e32 v74, 0x14800, v93
	v_add_u32_e32 v78, 0x15000, v93
	v_add_u32_e32 v82, 0x15800, v93
	s_waitcnt lgkmcnt(0)
	v_mfma_f32_16x16x32_f16 v[6:9], v[38:41], v[14:17], v[6:9]
	ds_read_b128 v[58:61], v58
	ds_read_b128 v[66:69], v66
	v_mfma_f32_16x16x32_f16 v[34:37], v[42:45], v[14:17], v[34:37]
	ds_read_b128 v[70:73], v70
	ds_read_b128 v[74:77], v74
	v_mfma_f32_16x16x32_f16 v[46:49], v[50:53], v[14:17], v[46:49]
	ds_read_b128 v[78:81], v78
	ds_read_b128 v[82:85], v82
	v_mfma_f32_16x16x32_f16 v[10:13], v[54:57], v[14:17], v[10:13]
	v_mfma_f32_16x16x32_f16 v[14:17], v[38:41], v[30:33], v[22:25]
	v_mfma_f32_16x16x32_f16 v[18:21], v[42:45], v[30:33], v[18:21]
	v_mfma_f32_16x16x32_f16 v[22:25], v[50:53], v[30:33], v[26:29]
	v_mfma_f32_16x16x32_f16 v[2:5], v[54:57], v[30:33], v[2:5]
	s_waitcnt vmcnt(0) lgkmcnt(0)
	s_waitcnt lgkmcnt(0)
	v_mfma_f32_16x16x32_f16 v[6:9], v[70:73], v[58:61], v[6:9]
	s_barrier
	ds_read_b128 v[26:29], v65
	ds_read_b128 v[30:33], v65 offset:2048
	v_mfma_f32_16x16x32_f16 v[34:37], v[74:77], v[58:61], v[34:37]
	ds_read_b128 v[38:41], v64 offset:16384
	ds_read_b128 v[42:45], v64 offset:18432
	v_mfma_f32_16x16x32_f16 v[46:49], v[78:81], v[58:61], v[46:49]
	ds_read_b128 v[50:53], v64 offset:20480
	ds_read_b128 v[54:57], v64 offset:22528
	v_mfma_f32_16x16x32_f16 v[10:13], v[82:85], v[58:61], v[10:13]
	v_mfma_f32_16x16x32_f16 v[14:17], v[70:73], v[66:69], v[14:17]
	v_mfma_f32_16x16x32_f16 v[18:21], v[74:77], v[66:69], v[18:21]
	v_mfma_f32_16x16x32_f16 v[22:25], v[78:81], v[66:69], v[22:25]
	v_mfma_f32_16x16x32_f16 v[2:5], v[82:85], v[66:69], v[2:5]
	s_waitcnt lgkmcnt(0)
	v_mfma_f32_16x16x32_f16 v[6:9], v[38:41], v[26:29], v[6:9]
	ds_read_b128 v[58:61], v93 offset:18432
	s_lshl_b64 s[0:1], s[0:1], 2
	v_lshl_add_u32 v63, v63, 5, s2
	v_mfma_f32_16x16x32_f16 v[34:37], v[42:45], v[26:29], v[34:37]
	s_add_u32 s0, s8, s0
	v_and_or_b32 v0, v0, 15, v63
	s_addc_u32 s1, s9, s1
	v_mfma_f32_16x16x32_f16 v[46:49], v[50:53], v[26:29], v[46:49]
	v_and_b32_e32 v1, 12, v1
	v_mfma_f32_16x16x32_f16 v[10:13], v[54:57], v[26:29], v[10:13]
	ds_read_b128 v[26:29], v92
	v_mfma_f32_16x16x32_f16 v[14:17], v[38:41], v[30:33], v[14:17]
	ds_read_b128 v[38:41], v92 offset:2048
	v_mfma_f32_16x16x32_f16 v[18:21], v[42:45], v[30:33], v[18:21]
	ds_read_b128 v[42:45], v93 offset:16384
	v_mfma_f32_16x16x32_f16 v[22:25], v[50:53], v[30:33], v[22:25]
	ds_read_b128 v[50:53], v93 offset:20480
	ds_read_b128 v[64:67], v93 offset:22528
	v_mfma_f32_16x16x32_f16 v[2:5], v[54:57], v[30:33], v[2:5]
	v_lshlrev_b32_e32 v54, 8, v62
	v_mov_b32_e32 v55, 0
	v_lshl_add_u64 v[56:57], s[0:1], 0, v[54:55]
	s_waitcnt lgkmcnt(0)
	v_mfma_f32_16x16x32_f16 v[6:9], v[42:45], v[26:29], v[6:9]
	v_lshlrev_b32_e32 v54, 2, v1
	v_ashrrev_i32_e32 v1, 31, v0
	v_mfma_f32_16x16x32_f16 v[10:13], v[64:67], v[26:29], v[10:13]
	v_mfma_f32_16x16x32_f16 v[30:33], v[58:61], v[26:29], v[34:37]
	v_mfma_f32_16x16x32_f16 v[34:37], v[50:53], v[26:29], v[46:49]
	s_nop 2
	v_lshlrev_b64 v[48:49], 12, v[0:1]
	v_or_b32_e32 v0, 16, v0
	v_lshl_add_u64 v[46:47], v[56:57], 0, v[54:55]
	v_ashrrev_i32_e32 v1, 31, v0
	v_lshl_add_u64 v[26:27], v[46:47], 0, v[48:49]
	v_lshlrev_b64 v[0:1], 12, v[0:1]
	global_store_dwordx4 v[26:27], v[6:9], off sc1
	global_store_dwordx4 v[26:27], v[10:13], off offset:192 sc1
	global_store_dwordx4 v[26:27], v[30:33], off offset:64 sc1
	v_mfma_f32_16x16x32_f16 v[6:9], v[42:45], v[38:41], v[14:17]
	global_store_dwordx4 v[26:27], v[34:37], off offset:128 sc1
	v_mfma_f32_16x16x32_f16 v[10:13], v[58:61], v[38:41], v[18:21]
	s_nop 2
	v_lshl_add_u64 v[18:19], v[46:47], 0, v[0:1]
	v_mfma_f32_16x16x32_f16 v[14:17], v[50:53], v[38:41], v[22:25]
	s_nop 0
	global_store_dwordx4 v[18:19], v[6:9], off sc1
	s_nop 0
	global_store_dwordx4 v[18:19], v[10:13], off offset:64 sc1
	v_mfma_f32_16x16x32_f16 v[0:3], v[64:67], v[38:41], v[2:5]
	s_nop 2
	global_store_dwordx4 v[18:19], v[14:17], off offset:128 sc1
	s_nop 3
	global_store_dwordx4 v[18:19], v[0:3], off offset:192 sc1
	s_endpgm

	.amdhsa_kernel _Z9gemm_gldsILi128ELi128ELi4ELi2ELi3ELi8ELi4ELi1ELi4096ELi1024ELi1024EEvPKDF16_S1_PfPKfS4_PKiPDF16_S7_S7_
		.amdhsa_group_segment_fixed_size 98304
		.amdhsa_private_segment_fixed_size 0
		.amdhsa_kernarg_size 72
		.amdhsa_user_sgpr_count 2
		.amdhsa_user_sgpr_dispatch_ptr 0
		.amdhsa_user_sgpr_queue_ptr 0
		.amdhsa_user_sgpr_kernarg_segment_ptr 1
		.amdhsa_user_sgpr_dispatch_id 0
		.amdhsa_user_sgpr_kernarg_preload_length 0
		.amdhsa_user_sgpr_kernarg_preload_offset 0
		.amdhsa_user_sgpr_private_segment_size 0
		.amdhsa_uses_dynamic_stack 0
		.amdhsa_enable_private_segment 0
		.amdhsa_system_sgpr_workgroup_id_x 1
		.amdhsa_system_sgpr_workgroup_id_y 0
		.amdhsa_system_sgpr_workgroup_id_z 0
		.amdhsa_system_sgpr_workgroup_info 0
		.amdhsa_system_vgpr_workitem_id 0
		.amdhsa_next_free_vgpr 169
		.amdhsa_next_free_sgpr 96
		.amdhsa_accum_offset 96
		.amdhsa_reserve_vcc 0
		.amdhsa_float_round_mode_32 0
		.amdhsa_float_round_mode_16_64 0
		.amdhsa_float_denorm_mode_32 3
		.amdhsa_float_denorm_mode_16_64 3
		.amdhsa_dx10_clamp 1
		.amdhsa_ieee_mode 1
		.amdhsa_fp16_overflow 0
		.amdhsa_tg_split 0
		.amdhsa_exception_fp_ieee_invalid_op 0
		.amdhsa_exception_fp_denorm_src 0
		.amdhsa_exception_fp_ieee_div_zero 0
		.amdhsa_exception_fp_ieee_overflow 0
		.amdhsa_exception_fp_ieee_underflow 0
		.amdhsa_exception_fp_ieee_inexact 0
		.amdhsa_exception_int_div_zero 0
	.end_amdhsa_kernel
